# baseline (speedup 1.0000x reference)
.Lco_nopoll:
	s_waitcnt lgkmcnt(0)
	s_barrier
	v_mov_b32_e32 v76, 0
	v_mov_b32_e32 v77, 0
	v_mov_b32_e32 v78, 0
	v_mov_b32_e32 v79, 0
	ds_write_b128 v74, v[76:79]
	ds_write_b128 v74, v[76:79] offset:8192
	ds_write_b128 v74, v[76:79] offset:16384
	ds_write_b128 v74, v[76:79] offset:24576
	ds_write_b128 v74, v[76:79] offset:32768
	ds_write_b128 v74, v[76:79] offset:40960
	ds_write_b128 v74, v[76:79] offset:49152
	ds_write_b128 v74, v[76:79] offset:57344
	v_mov_b32_e32 v0, 0x26400
	v_lshl_add_u32 v0, v75, 5, v0
	ds_read_b128 v[36:39], v0
	ds_read_b128 v[40:43], v0 offset:16
	s_waitcnt lgkmcnt(0)
	v_or3_b32 v44, v36, v37, v38
	v_or3_b32 v44, v44, v39, v40
	v_or3_b32 v44, v44, v41, v42
	v_or_b32_e32 v44, v44, v43
	v_bfe_u32 v44, v44, 15, 1
	v_and_b32_e32 v36, 0x7f, v36
	v_and_b32_e32 v37, 0x7f, v37
	v_and_b32_e32 v38, 0x7f, v38
	v_and_b32_e32 v39, 0x7f, v39
	v_and_b32_e32 v40, 0x7f, v40
	v_and_b32_e32 v41, 0x7f, v41
	v_and_b32_e32 v42, 0x7f, v42
	v_and_b32_e32 v43, 0x7f, v43
	v_mov_b32_e32 v45, v36
	v_add_u32_e32 v46, v45, v37
	v_add_u32_e32 v47, v46, v38
	v_add_u32_e32 v48, v47, v39
	v_add_u32_e32 v49, v48, v40
	v_add_u32_e32 v50, v49, v41
	v_add_u32_e32 v51, v50, v42
	v_add_u32_e32 v52, v51, v43
	v_cmp_lt_u32_e32 vcc, 0x100, v52
	v_add_u32_e32 v53, 15, v52
	v_lshrrev_b32_e32 v53, 4, v53
	v_cndmask_b32_e64 v54, 0, 1, vcc
	v_or_b32_e32 v44, v44, v54
	v_mov_b32_e32 v55, 0x26c00
	v_cmp_eq_u32_e32 vcc, 0, v70
	s_and_saveexec_b64 s[14:15], vcc
	ds_max_u32 v55, v53
	ds_or_b32 v55, v44 offset:4
	s_mov_b64 exec, s[14:15]
	s_waitcnt lgkmcnt(0)
	s_barrier
	ds_read_b64 v[0:1], v55
	v_lshlrev_b32_e32 v56, 5, v45
	v_lshlrev_b32_e32 v57, 5, v46
	v_lshlrev_b32_e32 v58, 5, v47
	v_lshlrev_b32_e32 v59, 5, v48
	v_lshlrev_b32_e32 v60, 5, v49
	v_lshlrev_b32_e32 v61, 5, v50
	v_lshlrev_b32_e32 v62, 5, v51
	v_sub_u32_e32 v56, 0x800, v56
	v_sub_u32_e32 v57, 0x1000, v57
	v_sub_u32_e32 v58, 0x1800, v58
	v_sub_u32_e32 v59, 0x2000, v59
	v_sub_u32_e32 v60, 0x2800, v60
	v_sub_u32_e32 v61, 0x3000, v61
	v_sub_u32_e32 v62, 0x3800, v62
	v_add_u32_e32 v63, s3, v75
	v_lshlrev_b32_e32 v63, 14, v63
	v_add_u32_e32 v63, 0x800000, v63
	s_waitcnt lgkmcnt(0)
	v_readfirstlane_b32 s77, v0
	v_readfirstlane_b32 s36, v1
	s_add_i32 s77, s77, 0
	s_cmp_lg_u32 s36, 0
	s_cselect_b64 s[6:7], 0, -1
	s_cmp_gt_u32 s10, 3
	s_cbranch_scc1 .Lco_done
	s_cmp_lg_u32 s36, 0
	s_cbranch_scc1 .Lco_gen
	v_mov_b32_e32 v0, v70
	v_cmp_lt_u32_e64 s[12:13], v0, v52
	v_cmp_le_u32_e64 s[16:17], v45, v0
	v_cmp_le_u32_e64 s[18:19], v46, v0
	v_cmp_le_u32_e64 s[20:21], v47, v0
	v_cmp_le_u32_e64 s[22:23], v48, v0
	v_cmp_le_u32_e64 s[24:25], v49, v0
	v_cmp_le_u32_e64 s[26:27], v50, v0
	v_cmp_le_u32_e64 s[28:29], v51, v0
	v_cndmask_b32_e64 v1, 0, v56, s[16:17]
	v_cndmask_b32_e64 v1, v1, v57, s[18:19]
	v_cndmask_b32_e64 v1, v1, v58, s[20:21]
	v_cndmask_b32_e64 v1, v1, v59, s[22:23]
	v_cndmask_b32_e64 v1, v1, v60, s[24:25]
	v_cndmask_b32_e64 v1, v1, v61, s[26:27]
	v_cndmask_b32_e64 v1, v1, v62, s[28:29]
	v_lshl_add_u32 v2, v0, 5, v63
	v_add_u32_e32 v2, v2, v1
	s_and_saveexec_b64 s[30:31], s[12:13]
	s_cbranch_execz .Lco_nold0
	global_load_dwordx4 v[208:211], v2, s[66:67] sc1
	global_load_dword v71, v2, s[66:67] offset:16 sc1
	v_mov_b32_e32 v18, 1.0
